# v13 + write-through (sc1) stores for the weight images converted at the end of phase 4, so the phase-4 split barrier finds less dirty L2 to write back
# speedup vs baseline: 1.0001x; 1.0001x over previous
.LBB0_1426:
	s_movk_i32 s19, 0x84
	v_lshlrev_b32_e32 v16, 2, v27
	v_mul_lo_u32 v25, v28, s19
	v_add3_u32 v16, s38, v16, v25
	v_add_u32_e32 v93, 0x400, v16
	v_add_u32_e32 v94, 0x800, v16
	v_add_u32_e32 v95, 0xc00, v16
	v_add_u32_e32 v96, 0x1000, v16
	s_waitcnt vmcnt(0) lgkmcnt(0)
	ds_write2_b32 v16, v29, v30 offset1:66
	ds_write2_b32 v16, v31, v33 offset0:132 offset1:198
	ds_write2_b32 v93, v32, v34 offset0:8 offset1:74
	ds_write2_b32 v93, v35, v36 offset0:140 offset1:206
	ds_write2_b32 v94, v37, v38 offset0:16 offset1:82
	ds_write2_b32 v94, v39, v40 offset0:148 offset1:214
	ds_write2_b32 v95, v41, v42 offset0:24 offset1:90
	ds_write2_b32 v95, v43, v44 offset0:156 offset1:222
	ds_write2_b32 v96, v45, v46 offset0:32 offset1:98
	ds_write2_b32 v96, v47, v48 offset0:164 offset1:230
	v_add_u32_e32 v48, 0x1400, v16
	ds_write2_b32 v48, v49, v50 offset0:40 offset1:106
	ds_write2_b32 v48, v51, v52 offset0:172 offset1:238
	v_add_u32_e32 v49, 0x1800, v16
	v_add_u32_e32 v50, 0x1c00, v16
	ds_write2_b32 v49, v53, v54 offset0:48 offset1:114
	ds_write2_b32 v49, v55, v56 offset0:180 offset1:246
	ds_write2_b32 v50, v57, v58 offset0:56 offset1:122
	ds_write2_b32 v50, v59, v60 offset0:188 offset1:254
	v_ashrrev_i32_e32 v51, 3, v26
	s_waitcnt lgkmcnt(0)
	v_mul_u32_u24_e32 v24, 0x84, v24
	v_lshlrev_b32_e32 v25, 2, v51
	v_add3_u32 v52, s38, v24, v25
	ds_read2_b32 v[28:29], v52 offset1:8
	ds_read2_b32 v[30:31], v52 offset0:66 offset1:74
	ds_read2_b32 v[32:33], v52 offset0:33 offset1:41
	ds_read2_b32 v[34:35], v52 offset0:99 offset1:107
	ds_read2_b32 v[36:37], v52 offset0:132 offset1:140
	ds_read2_b32 v[38:39], v52 offset0:198 offset1:206
	ds_read2_b32 v[40:41], v52 offset0:165 offset1:173
	ds_read2_b32 v[42:43], v52 offset0:231 offset1:239
	s_waitcnt lgkmcnt(7)
	v_mov_b32_e32 v24, v28
	s_waitcnt lgkmcnt(5)
	v_mov_b32_e32 v26, v32
	s_waitcnt lgkmcnt(4)
	v_mov_b32_e32 v27, v34
	s_waitcnt lgkmcnt(3)
	v_mov_b32_e32 v44, v36
	s_waitcnt lgkmcnt(2)
	v_mov_b32_e32 v45, v38
	s_waitcnt lgkmcnt(1)
	v_mov_b32_e32 v46, v40
	s_waitcnt lgkmcnt(0)
	v_mov_b32_e32 v47, v42
	v_mov_b32_e32 v25, v30
	v_pk_mul_f32 v[26:27], v[18:19], v[26:27]
	v_pk_mul_f32 v[44:45], v[6:7], v[44:45]
	v_pk_mul_f32 v[46:47], v[4:5], v[46:47]
	v_pk_mul_f32 v[24:25], v[2:3], v[24:25]
	v_bfe_u32 v28, v47, 16, 1
	v_bfe_u32 v32, v27, 16, 1
	v_bfe_u32 v36, v44, 16, 1
	v_bfe_u32 v30, v46, 16, 1
	v_bfe_u32 v34, v26, 16, 1
	v_add3_u32 v32, v27, v32, s97
	v_add3_u32 v27, v47, v28, s97
	v_bfe_u32 v28, v24, 16, 1
	v_bfe_u32 v38, v45, 16, 1
	v_add3_u32 v36, v44, v36, s97
	v_add3_u32 v34, v26, v34, s97
	v_add3_u32 v26, v46, v30, s97
	v_bfe_u32 v30, v25, 16, 1
	v_add3_u32 v38, v45, v38, s97
	v_add3_u32 v24, v24, v28, s97
	v_lshrrev_b32_e32 v28, 16, v36
	v_add3_u32 v25, v25, v30, s97
	v_lshrrev_b32_e32 v30, 16, v38
	v_and_or_b32 v26, v26, s88, v28
	v_add_u32_e32 v28, s33, v51
	v_lshrrev_b32_e32 v25, 16, v25
	v_and_or_b32 v27, v27, s88, v30
	v_ashrrev_i32_e32 v30, 31, v28
	v_and_or_b32 v25, v32, s88, v25
	v_mul_lo_u32 v30, s14, v30
	v_mul_lo_u32 v32, s15, v28
	v_mad_u64_u32 v[44:45], s[24:25], s14, v28, 0
	v_add3_u32 v45, v45, v30, v32
	s_ashr_i32 s19, s18, 31
	v_lshl_add_u64 v[44:45], v[44:45], 1, s[16:17]
	s_lshl_b64 s[18:19], s[18:19], 1
	v_lshrrev_b32_e32 v24, 16, v24
	v_lshl_add_u64 v[44:45], v[44:45], 0, s[18:19]
	v_lshlrev_b64 v[12:13], 1, v[12:13]
	v_and_or_b32 v24, v34, s88, v24
	v_lshl_add_u64 v[44:45], v[44:45], 0, v[12:13]
	v_mov_b32_e32 v30, v29
	v_mov_b32_e32 v34, v33
	v_mov_b32_e32 v42, v41
	global_store_dwordx4 v[44:45], v[24:27], off sc1
	v_mov_b32_e32 v38, v37
	v_pk_mul_f32 v[28:29], v[6:7], v[38:39]
	v_pk_mul_f32 v[24:25], v[2:3], v[30:31]
	v_pk_mul_f32 v[26:27], v[18:19], v[34:35]
	v_pk_mul_f32 v[30:31], v[4:5], v[42:43]
	v_bfe_u32 v34, v27, 16, 1
	v_bfe_u32 v32, v31, 16, 1
	v_bfe_u32 v33, v30, 16, 1
	v_bfe_u32 v35, v26, 16, 1
	v_add3_u32 v34, v27, v34, s97
	v_add3_u32 v27, v31, v32, s97
	v_bfe_u32 v32, v28, 16, 1
	v_add3_u32 v35, v26, v35, s97
	v_add3_u32 v26, v30, v33, s97
	v_bfe_u32 v33, v29, 16, 1
	v_add3_u32 v28, v28, v32, s97
	v_add_u32_e32 v53, 8, v51
	v_add3_u32 v29, v29, v33, s97
	v_lshrrev_b32_e32 v28, 16, v28
	v_lshrrev_b32_e32 v29, 16, v29
	v_and_or_b32 v26, v26, s88, v28
	v_add_u32_e32 v28, s33, v53
	v_bfe_u32 v30, v24, 16, 1
	v_bfe_u32 v31, v25, 16, 1
	v_and_or_b32 v27, v27, s88, v29
	v_ashrrev_i32_e32 v29, 31, v28
	v_add3_u32 v25, v25, v31, s97
	v_add3_u32 v24, v24, v30, s97
	v_mul_lo_u32 v30, s14, v29
	v_mul_lo_u32 v31, s15, v28
	v_mad_u64_u32 v[28:29], s[24:25], s14, v28, 0
	v_add3_u32 v29, v29, v30, v31
	v_lshl_add_u64 v[28:29], v[28:29], 1, s[16:17]
	v_lshrrev_b32_e32 v24, 16, v24
	v_lshrrev_b32_e32 v25, 16, v25
	v_lshl_add_u64 v[28:29], v[28:29], 0, s[18:19]
	v_and_or_b32 v25, v34, s88, v25
	v_and_or_b32 v24, v35, s88, v24
	v_lshl_add_u64 v[28:29], v[28:29], 0, v[12:13]
	global_store_dwordx4 v[28:29], v[24:27], off sc1
	ds_read2_b32 v[28:29], v52 offset0:16 offset1:24
	ds_read2_b32 v[30:31], v52 offset0:82 offset1:90
	ds_read2_b32 v[32:33], v52 offset0:49 offset1:57
	ds_read2_b32 v[34:35], v52 offset0:115 offset1:123
	ds_read2_b32 v[36:37], v52 offset0:148 offset1:156
	ds_read2_b32 v[38:39], v52 offset0:214 offset1:222
	ds_read2_b32 v[40:41], v52 offset0:181 offset1:189
	ds_read2_b32 v[42:43], v52 offset0:247 offset1:255
	s_waitcnt lgkmcnt(7)
	v_mov_b32_e32 v24, v28
	s_waitcnt lgkmcnt(5)
	v_mov_b32_e32 v26, v32
	s_waitcnt lgkmcnt(4)
	v_mov_b32_e32 v27, v34
	s_waitcnt lgkmcnt(3)
	v_mov_b32_e32 v44, v36
	s_waitcnt lgkmcnt(2)
	v_mov_b32_e32 v45, v38
	s_waitcnt lgkmcnt(1)
	v_mov_b32_e32 v46, v40
	s_waitcnt lgkmcnt(0)
	v_mov_b32_e32 v47, v42
	v_mov_b32_e32 v25, v30
	v_pk_mul_f32 v[26:27], v[18:19], v[26:27]
	v_pk_mul_f32 v[44:45], v[6:7], v[44:45]
	v_pk_mul_f32 v[46:47], v[4:5], v[46:47]
	v_pk_mul_f32 v[24:25], v[2:3], v[24:25]
	v_bfe_u32 v28, v47, 16, 1
	v_bfe_u32 v32, v27, 16, 1
	v_bfe_u32 v36, v44, 16, 1
	v_bfe_u32 v30, v46, 16, 1
	v_bfe_u32 v34, v26, 16, 1
	v_add3_u32 v32, v27, v32, s97
	v_add3_u32 v27, v47, v28, s97
	v_bfe_u32 v28, v24, 16, 1
	v_bfe_u32 v38, v45, 16, 1
	v_add3_u32 v36, v44, v36, s97
	v_add_u32_e32 v54, 16, v51
	v_add3_u32 v34, v26, v34, s97
	v_add3_u32 v26, v46, v30, s97
	v_bfe_u32 v30, v25, 16, 1
	v_add3_u32 v38, v45, v38, s97
	v_add3_u32 v24, v24, v28, s97
	v_lshrrev_b32_e32 v28, 16, v36
	v_add3_u32 v25, v25, v30, s97
	v_lshrrev_b32_e32 v30, 16, v38
	v_and_or_b32 v26, v26, s88, v28
	v_add_u32_e32 v28, s33, v54
	v_lshrrev_b32_e32 v25, 16, v25
	v_and_or_b32 v27, v27, s88, v30
	v_ashrrev_i32_e32 v30, 31, v28
	v_and_or_b32 v25, v32, s88, v25
	v_mul_lo_u32 v30, s14, v30
	v_mul_lo_u32 v32, s15, v28
	v_mad_u64_u32 v[44:45], s[24:25], s14, v28, 0
	v_add3_u32 v45, v45, v30, v32
	v_lshrrev_b32_e32 v24, 16, v24
	v_lshl_add_u64 v[44:45], v[44:45], 1, s[16:17]
	v_and_or_b32 v24, v34, s88, v24
	v_lshl_add_u64 v[44:45], v[44:45], 0, s[18:19]
	v_mov_b32_e32 v34, v33
	v_lshl_add_u64 v[44:45], v[44:45], 0, v[12:13]
	v_pk_mul_f32 v[18:19], v[18:19], v[34:35]
	v_mov_b32_e32 v38, v37
	global_store_dwordx4 v[44:45], v[24:27], off sc1
	v_pk_mul_f32 v[6:7], v[6:7], v[38:39]
	v_mov_b32_e32 v42, v41
	v_bfe_u32 v26, v19, 16, 1
	v_mov_b32_e32 v30, v29
	v_pk_mul_f32 v[4:5], v[4:5], v[42:43]
	v_bfe_u32 v27, v18, 16, 1
	v_add3_u32 v19, v19, v26, s97
	v_bfe_u32 v26, v6, 16, 1
	v_pk_mul_f32 v[2:3], v[2:3], v[30:31]
	v_bfe_u32 v24, v5, 16, 1
	v_bfe_u32 v25, v4, 16, 1
	v_add3_u32 v18, v18, v27, s97
	v_bfe_u32 v27, v7, 16, 1
	v_add3_u32 v6, v6, v26, s97
	v_add_u32_e32 v40, 24, v51
	v_add3_u32 v4, v4, v25, s97
	v_add3_u32 v5, v5, v24, s97
	v_bfe_u32 v24, v2, 16, 1
	v_bfe_u32 v25, v3, 16, 1
	v_add3_u32 v7, v7, v27, s97
	v_lshrrev_b32_e32 v6, 16, v6
	v_add3_u32 v3, v3, v25, s97
	v_add3_u32 v2, v2, v24, s97
	v_lshrrev_b32_e32 v7, 16, v7
	v_and_or_b32 v4, v4, s88, v6
	v_add_u32_e32 v6, s33, v40
	v_lshrrev_b32_e32 v2, 16, v2
	v_lshrrev_b32_e32 v3, 16, v3
	v_and_or_b32 v5, v5, s88, v7
	v_ashrrev_i32_e32 v7, 31, v6
	v_and_or_b32 v3, v19, s88, v3
	v_and_or_b32 v2, v18, s88, v2
	v_mul_lo_u32 v18, s14, v7
	v_mul_lo_u32 v19, s15, v6
	v_mad_u64_u32 v[6:7], s[14:15], s14, v6, 0
	v_add3_u32 v7, v7, v18, v19
	v_lshl_add_u64 v[6:7], v[6:7], 1, s[16:17]
	v_lshl_add_u64 v[6:7], v[6:7], 0, s[18:19]
	v_lshl_add_u64 v[6:7], v[6:7], 0, v[12:13]
	global_store_dwordx4 v[6:7], v[2:5], off sc1
	s_waitcnt lgkmcnt(0)
	ds_write2_b32 v16, v61, v62 offset1:66
	ds_write2_b32 v16, v63, v64 offset0:132 offset1:198
	ds_write2_b32 v93, v65, v66 offset0:8 offset1:74
	ds_write2_b32 v93, v67, v68 offset0:140 offset1:206
	ds_write2_b32 v94, v69, v70 offset0:16 offset1:82
	ds_write2_b32 v94, v71, v72 offset0:148 offset1:214
	ds_write2_b32 v95, v73, v74 offset0:24 offset1:90
	ds_write2_b32 v95, v75, v76 offset0:156 offset1:222
	ds_write2_b32 v96, v77, v78 offset0:32 offset1:98
	ds_write2_b32 v96, v79, v80 offset0:164 offset1:230
	ds_write2_b32 v48, v81, v82 offset0:40 offset1:106
	ds_write2_b32 v48, v83, v84 offset0:172 offset1:238
	ds_write2_b32 v49, v85, v86 offset0:48 offset1:114
	ds_write2_b32 v49, v87, v88 offset0:180 offset1:246
	ds_write2_b32 v50, v89, v90 offset0:56 offset1:122
	ds_write2_b32 v50, v91, v92 offset0:188 offset1:254
	s_waitcnt lgkmcnt(0)
	ds_read2_b32 v[6:7], v52 offset1:8
	ds_read2_b32 v[18:19], v52 offset0:66 offset1:74
	ds_read2_b32 v[24:25], v52 offset0:33 offset1:41
	ds_read2_b32 v[26:27], v52 offset0:99 offset1:107
	ds_read2_b32 v[28:29], v52 offset0:132 offset1:140
	ds_read2_b32 v[30:31], v52 offset0:198 offset1:206
	ds_read2_b32 v[32:33], v52 offset0:165 offset1:173
	ds_read2_b32 v[34:35], v52 offset0:231 offset1:239
	s_waitcnt lgkmcnt(7)
	v_mov_b32_e32 v2, v6
	s_waitcnt lgkmcnt(5)
	v_mov_b32_e32 v4, v24
	s_waitcnt lgkmcnt(4)
	v_mov_b32_e32 v5, v26
	s_waitcnt lgkmcnt(3)
	v_mov_b32_e32 v36, v28
	s_waitcnt lgkmcnt(2)
	v_mov_b32_e32 v37, v30
	s_waitcnt lgkmcnt(1)
	v_mov_b32_e32 v38, v32
	s_waitcnt lgkmcnt(0)
	v_mov_b32_e32 v39, v34
	v_mov_b32_e32 v3, v18
	v_pk_mul_f32 v[4:5], v[14:15], v[4:5]
	v_pk_mul_f32 v[36:37], v[20:21], v[36:37]
	v_pk_mul_f32 v[38:39], v[10:11], v[38:39]
	v_pk_mul_f32 v[2:3], v[8:9], v[2:3]
	v_bfe_u32 v6, v39, 16, 1
	v_bfe_u32 v18, v5, 16, 1
	v_bfe_u32 v26, v36, 16, 1
	v_bfe_u32 v16, v38, 16, 1
	v_bfe_u32 v24, v4, 16, 1
	v_add3_u32 v18, v5, v18, s97
	v_add3_u32 v5, v39, v6, s97
	v_bfe_u32 v6, v2, 16, 1
	v_bfe_u32 v28, v37, 16, 1
	v_add3_u32 v26, v36, v26, s97
	v_add3_u32 v24, v4, v24, s97
	v_add3_u32 v4, v38, v16, s97
	v_bfe_u32 v16, v3, 16, 1
	v_add3_u32 v28, v37, v28, s97
	v_add3_u32 v2, v2, v6, s97
	v_lshrrev_b32_e32 v6, 16, v26
	v_add3_u32 v3, v3, v16, s97
	v_lshrrev_b32_e32 v16, 16, v28
	v_and_or_b32 v4, v4, s88, v6
	v_add_u32_e32 v6, s90, v51
	v_lshrrev_b32_e32 v3, 16, v3
	v_and_or_b32 v5, v5, s88, v16
	v_ashrrev_i32_e32 v16, 31, v6
	v_and_or_b32 v3, v18, s88, v3
	v_mul_lo_u32 v16, s20, v16
	v_mul_lo_u32 v18, s21, v6
	v_mad_u64_u32 v[36:37], s[14:15], s20, v6, 0
	v_add3_u32 v37, v37, v16, v18
	v_lshl_add_u64 v[36:37], v[36:37], 1, s[22:23]
	v_lshlrev_b64 v[22:23], 1, v[22:23]
	v_lshrrev_b32_e32 v2, 16, v2
	v_lshl_add_u64 v[36:37], v[36:37], 0, v[22:23]
	v_and_or_b32 v2, v24, s88, v2
	v_lshl_add_u64 v[36:37], v[36:37], 0, v[12:13]
	v_mov_b32_e32 v18, v7
	v_mov_b32_e32 v26, v25
	v_mov_b32_e32 v34, v33
	global_store_dwordx4 v[36:37], v[2:5], off sc1
	v_mov_b32_e32 v30, v29
	v_pk_mul_f32 v[6:7], v[20:21], v[30:31]
	v_pk_mul_f32 v[2:3], v[8:9], v[18:19]
	v_pk_mul_f32 v[4:5], v[14:15], v[26:27]
	v_pk_mul_f32 v[18:19], v[10:11], v[34:35]
	v_bfe_u32 v25, v5, 16, 1
	v_bfe_u32 v16, v19, 16, 1
	v_bfe_u32 v24, v18, 16, 1
	v_bfe_u32 v26, v4, 16, 1
	v_add3_u32 v25, v5, v25, s97
	v_add3_u32 v5, v19, v16, s97
	v_bfe_u32 v19, v6, 16, 1
	v_add3_u32 v26, v4, v26, s97
	v_add3_u32 v4, v18, v24, s97
	v_bfe_u32 v24, v7, 16, 1
	v_add3_u32 v6, v6, v19, s97
	v_add3_u32 v7, v7, v24, s97
	v_lshrrev_b32_e32 v6, 16, v6
	v_lshrrev_b32_e32 v7, 16, v7
	v_and_or_b32 v4, v4, s88, v6
	v_add_u32_e32 v6, s90, v53
	v_bfe_u32 v16, v2, 16, 1
	v_bfe_u32 v18, v3, 16, 1
	v_and_or_b32 v5, v5, s88, v7
	v_ashrrev_i32_e32 v7, 31, v6
	v_add3_u32 v3, v3, v18, s97
	v_add3_u32 v2, v2, v16, s97
	v_mul_lo_u32 v16, s20, v7
	v_mul_lo_u32 v18, s21, v6
	v_mad_u64_u32 v[6:7], s[14:15], s20, v6, 0
	v_add3_u32 v7, v7, v16, v18
	v_lshl_add_u64 v[6:7], v[6:7], 1, s[22:23]
	v_lshrrev_b32_e32 v2, 16, v2
	v_lshrrev_b32_e32 v3, 16, v3
	v_lshl_add_u64 v[6:7], v[6:7], 0, v[22:23]
	v_and_or_b32 v3, v25, s88, v3
	v_and_or_b32 v2, v26, s88, v2
	v_lshl_add_u64 v[6:7], v[6:7], 0, v[12:13]
	ds_read2_b32 v[18:19], v52 offset0:16 offset1:24
	ds_read2_b32 v[24:25], v52 offset0:82 offset1:90
	global_store_dwordx4 v[6:7], v[2:5], off sc1
	ds_read2_b32 v[6:7], v52 offset0:49 offset1:57
	ds_read2_b32 v[26:27], v52 offset0:115 offset1:123
	ds_read2_b32 v[28:29], v52 offset0:148 offset1:156
	ds_read2_b32 v[30:31], v52 offset0:214 offset1:222
	ds_read2_b32 v[32:33], v52 offset0:181 offset1:189
	ds_read2_b32 v[34:35], v52 offset0:247 offset1:255
	s_waitcnt lgkmcnt(7)
	v_mov_b32_e32 v2, v18
	s_waitcnt lgkmcnt(5)
	v_mov_b32_e32 v4, v6
	s_waitcnt lgkmcnt(4)
	v_mov_b32_e32 v5, v26
	s_waitcnt lgkmcnt(3)
	v_mov_b32_e32 v36, v28
	s_waitcnt lgkmcnt(2)
	v_mov_b32_e32 v37, v30
	s_waitcnt lgkmcnt(1)
	v_mov_b32_e32 v38, v32
	s_waitcnt lgkmcnt(0)
	v_mov_b32_e32 v39, v34
	v_mov_b32_e32 v3, v24
	v_pk_mul_f32 v[4:5], v[14:15], v[4:5]
	v_pk_mul_f32 v[36:37], v[20:21], v[36:37]
	v_pk_mul_f32 v[38:39], v[10:11], v[38:39]
	v_pk_mul_f32 v[2:3], v[8:9], v[2:3]
	v_bfe_u32 v6, v39, 16, 1
	v_bfe_u32 v18, v5, 16, 1
	v_bfe_u32 v26, v36, 16, 1
	v_bfe_u32 v16, v38, 16, 1
	v_bfe_u32 v24, v4, 16, 1
	v_add3_u32 v18, v5, v18, s97
	v_add3_u32 v5, v39, v6, s97
	v_bfe_u32 v6, v2, 16, 1
	v_bfe_u32 v28, v37, 16, 1
	v_add3_u32 v26, v36, v26, s97
	v_add3_u32 v24, v4, v24, s97
	v_add3_u32 v4, v38, v16, s97
	v_bfe_u32 v16, v3, 16, 1
	v_add3_u32 v28, v37, v28, s97
	v_add3_u32 v2, v2, v6, s97
	v_lshrrev_b32_e32 v6, 16, v26
	v_add3_u32 v3, v3, v16, s97
	v_lshrrev_b32_e32 v16, 16, v28
	v_and_or_b32 v4, v4, s88, v6
	v_add_u32_e32 v6, s90, v54
	v_lshrrev_b32_e32 v3, 16, v3
	v_and_or_b32 v5, v5, s88, v16
	v_ashrrev_i32_e32 v16, 31, v6
	v_and_or_b32 v3, v18, s88, v3
	v_mul_lo_u32 v16, s20, v16
	v_mul_lo_u32 v18, s21, v6
	v_mad_u64_u32 v[36:37], s[14:15], s20, v6, 0
	v_add3_u32 v37, v37, v16, v18
	v_lshl_add_u64 v[36:37], v[36:37], 1, s[22:23]
	v_lshrrev_b32_e32 v2, 16, v2
	v_lshl_add_u64 v[36:37], v[36:37], 0, v[22:23]
	v_and_or_b32 v2, v24, s88, v2
	v_lshl_add_u64 v[36:37], v[36:37], 0, v[12:13]
	v_mov_b32_e32 v24, v19
	v_mov_b32_e32 v26, v7
	v_mov_b32_e32 v34, v33
	global_store_dwordx4 v[36:37], v[2:5], off sc1
	v_mov_b32_e32 v30, v29
	v_pk_mul_f32 v[6:7], v[20:21], v[30:31]
	v_pk_mul_f32 v[2:3], v[8:9], v[24:25]
	v_pk_mul_f32 v[4:5], v[14:15], v[26:27]
	v_pk_mul_f32 v[8:9], v[10:11], v[34:35]
	v_bfe_u32 v14, v5, 16, 1
	v_bfe_u32 v10, v9, 16, 1
	v_bfe_u32 v11, v8, 16, 1
	v_bfe_u32 v15, v4, 16, 1
	v_add3_u32 v14, v5, v14, s97
	v_add3_u32 v5, v9, v10, s97
	v_bfe_u32 v10, v6, 16, 1
	v_add3_u32 v15, v4, v15, s97
	v_add3_u32 v4, v8, v11, s97
	v_bfe_u32 v11, v7, 16, 1
	v_add3_u32 v6, v6, v10, s97
	v_add3_u32 v7, v7, v11, s97
	v_lshrrev_b32_e32 v6, 16, v6
	v_lshrrev_b32_e32 v7, 16, v7
	v_and_or_b32 v4, v4, s88, v6
	v_add_u32_e32 v6, s90, v40
	v_bfe_u32 v8, v2, 16, 1
	v_bfe_u32 v9, v3, 16, 1
	v_and_or_b32 v5, v5, s88, v7
	v_ashrrev_i32_e32 v7, 31, v6
	v_add3_u32 v3, v3, v9, s97
	v_add3_u32 v2, v2, v8, s97
	v_mul_lo_u32 v8, s20, v7
	v_mul_lo_u32 v9, s21, v6
	v_mad_u64_u32 v[6:7], s[14:15], s20, v6, 0
	v_add3_u32 v7, v7, v8, v9
	v_lshl_add_u64 v[6:7], v[6:7], 1, s[22:23]
	v_lshrrev_b32_e32 v2, 16, v2
	v_lshrrev_b32_e32 v3, 16, v3
	v_lshl_add_u64 v[6:7], v[6:7], 0, v[22:23]
	v_and_or_b32 v3, v14, s88, v3
	v_and_or_b32 v2, v15, s88, v2
	v_lshl_add_u64 v[6:7], v[6:7], 0, v[12:13]
	global_store_dwordx4 v[6:7], v[2:5], off sc1
	s_waitcnt lgkmcnt(0)
	s_mov_b64 s[14:15], 0
